# baseline (speedup 1.0000x reference)
.Lpro_wl_done:
	s_lshr_b32 s38, s30, 9
	s_lshl_b32 s38, s38, 4
	s_add_i32 s38, s38, s37
	s_mul_i32 s38, s38, 0xc00
	v_lshlrev_b32_e32 v27, 4, v1
	v_add_u32_e32 v27, s38, v27
	v_min_u32_e32 v28, 0x1387f0, v27
	global_load_dwordx4 v[124:127], v28, s[62:63] sc1
	v_add_u32_e32 v27, 0x400, v27
	v_min_u32_e32 v28, 0x1387f0, v27
	global_load_dwordx4 v[124:127], v28, s[62:63] sc1
	v_add_u32_e32 v27, 0x400, v27
	v_min_u32_e32 v28, 0x1387f0, v27
	global_load_dwordx4 v[124:127], v28, s[62:63] sc1
	s_waitcnt vmcnt(3)
	s_cmp_lg_u32 s37, 0
	s_cbranch_scc1 .Lpro_not_w0
	v_mov_b32_e32 v6, 0x15300
	v_lshl_add_u32 v6, v1, 2, v6
	ds_write_b32 v6, v16
	v_mov_b32_e32 v6, 0
	v_mov_b32_e32 v7, 0x15400
	ds_write_b32 v7, v6
